# v22 + software-pipelined convert loop (attention L0 first call): loads for item n+1 issued at loop top into second register set, claim-ahead
# baseline (speedup 1.0000x reference)
.LBB0_534:
	s_lshr_b32 s12, s30, 7
	v_cvt_f32_u32_e32 v112, s12
	s_sub_i32 s19, 0, s12
	s_abs_i32 s17, s10
	s_ashr_i32 s16, s10, 31
	v_rcp_iflag_f32_e32 v112, v112
	s_mov_b32 s31, 0
	v_lshlrev_b32_e32 v114, 2, v192
	v_mov_b32_e32 v115, 0
	v_mul_f32_e32 v112, 0x4f7ffffe, v112
	v_cvt_u32_f32_e32 v112, v112
	s_nop 0
	v_readfirstlane_b32 s21, v112
	s_mul_i32 s19, s19, s21
	s_mul_hi_u32 s19, s21, s19
	s_add_i32 s21, s21, s19
	s_mul_hi_u32 s19, s17, s21
	s_mul_i32 s21, s19, s12
	s_sub_i32 s17, s17, s21
	s_add_i32 s22, s19, 1
	s_sub_i32 s21, s17, s12
	s_cmp_ge_u32 s17, s12
	s_cselect_b32 s19, s22, s19
	s_cselect_b32 s17, s21, s17
	s_add_i32 s21, s19, 1
	s_cmp_ge_u32 s17, s12
	s_cselect_b32 s17, s21, s19
	s_xor_b32 s17, s17, s16
	s_sub_i32 s16, s17, s16
	s_mul_i32 s12, s16, s12
	s_lshl_b32 s21, s16, 8
	s_sub_i32 s10, s10, s12
	v_or_b32_e32 v112, s21, v196
	s_ashr_i32 s12, s21, 31
	s_mul_i32 s12, s12, s30
	v_mad_u64_u32 v[112:113], s[16:17], v112, s30, 0
	s_lshl_b32 s84, s10, 7
	v_add_u32_e32 v113, s12, v113
	v_lshl_add_u64 v[112:113], v[112:113], 2, s[6:7]
	s_ashr_i32 s85, s84, 31
	v_lshl_add_u64 v[112:113], s[84:85], 2, v[112:113]
	v_lshl_add_u64 v[112:113], v[112:113], 0, v[114:115]
	s_lshl_b64 s[6:7], s[30:31], 2
	v_lshl_add_u64 v[120:121], v[112:113], 0, s[6:7]
	global_load_dwordx4 v[112:115], v[112:113], off nt
	s_nop 0
	global_load_dwordx4 v[116:119], v[120:121], off nt
	v_lshl_add_u64 v[120:121], v[120:121], 0, s[6:7]
	v_lshl_add_u64 v[128:129], v[120:121], 0, s[6:7]
	global_load_dwordx4 v[120:123], v[120:121], off nt
	s_nop 0
	global_load_dwordx4 v[124:127], v[128:129], off nt
	v_lshl_add_u64 v[128:129], v[128:129], 0, s[6:7]
	v_lshl_add_u64 v[136:137], v[128:129], 0, s[6:7]
	global_load_dwordx4 v[128:131], v[128:129], off nt
	s_nop 0
	global_load_dwordx4 v[132:135], v[136:137], off nt
	v_lshl_add_u64 v[136:137], v[136:137], 0, s[6:7]
	v_lshl_add_u64 v[144:145], v[136:137], 0, s[6:7]
	v_lshl_add_u64 v[148:149], v[144:145], 0, s[6:7]
	v_lshl_add_u64 v[152:153], v[148:149], 0, s[6:7]
	v_lshl_add_u64 v[156:157], v[152:153], 0, s[6:7]
	v_lshl_add_u64 v[160:161], v[156:157], 0, s[6:7]
	s_waitcnt vmcnt(8)
	v_lshl_add_u64 v[164:165], v[160:161], 0, s[6:7]
	s_waitcnt vmcnt(7)
	v_lshl_add_u64 v[168:169], v[164:165], 0, s[6:7]
	s_waitcnt vmcnt(6)
	v_lshl_add_u64 v[172:173], v[168:169], 0, s[6:7]
	global_load_dwordx4 v[136:139], v[136:137], off nt
	s_nop 0
	global_load_dwordx4 v[140:143], v[144:145], off nt
	s_nop 0
	global_load_dwordx4 v[144:147], v[148:149], off nt
	s_nop 0
	global_load_dwordx4 v[148:151], v[152:153], off nt
	s_nop 0
	global_load_dwordx4 v[152:155], v[156:157], off nt
	s_nop 0
	global_load_dwordx4 v[156:159], v[160:161], off nt
	s_nop 0
	global_load_dwordx4 v[160:163], v[164:165], off nt
	s_nop 0
	global_load_dwordx4 v[164:167], v[168:169], off nt
	s_nop 0
	global_load_dwordx4 v[168:171], v[172:173], off nt
	v_lshl_add_u64 v[172:173], v[172:173], 0, s[6:7]
	global_load_dwordx4 v[172:175], v[172:173], off nt
	s_andn2_b64 vcc, exec, s[2:3]
	s_mov_b32 s16, 1
	s_cbranch_vccnz .LBB0_690
.LBB0_535:
	v_readlane_b32 s36, v254, 38
	v_readlane_b32 s50, v254, 52
	v_readlane_b32 s51, v254, 53
	s_add_u32 s17, s50, 0x27200000
	s_addc_u32 s53, s51, 0
	s_add_u32 s54, s50, 0xb200000
	s_addc_u32 s55, s51, 0
	s_add_u32 s6, s50, 0x9c00000
	s_addc_u32 s7, s51, 0
	s_add_u32 s56, s50, 0x7000000
	s_addc_u32 s57, s51, 0
	s_add_u32 s58, s50, 0x6000000
	s_addc_u32 s59, s51, 0
	s_add_u32 s60, s50, 0x5800000
	s_addc_u32 s61, s51, 0
	s_add_u32 s62, s50, 0x5000000
	s_addc_u32 s63, s51, 0
	s_add_u32 s64, s50, 0x800000
	s_addc_u32 s65, s51, 0
	s_mov_b32 s66, 0xc2fe0000
	s_mov_b32 s72, 0x4b400000
	s_mov_b32 s75, 0
	v_mov_b32_e32 v75, 0
	s_add_i32 s67, 0, 0x20184
	v_mov_b32_e32 v71, 0x42fe0000
	v_readlane_b32 s37, v254, 39
	v_readlane_b32 s38, v254, 40
	v_readlane_b32 s39, v254, 41
	v_readlane_b32 s40, v254, 42
	v_readlane_b32 s41, v254, 43
	v_readlane_b32 s42, v254, 44
	v_readlane_b32 s43, v254, 45
	v_readlane_b32 s44, v254, 46
	v_readlane_b32 s45, v254, 47
	v_readlane_b32 s46, v254, 48
	v_readlane_b32 s47, v254, 49
	v_readlane_b32 s48, v254, 50
	v_readlane_b32 s49, v254, 51
	s_and_saveexec_b64 s[2:3], s[0:1]
	s_cbranch_execz .LppA_pr
	v_readlane_b32 s30, v254, 52
	v_readlane_b32 s31, v254, 53
	v_mov_b32_e32 v253, 1
	s_nop 4
	global_atomic_add v253, v75, v253, s[30:31] offset:1280 sc0
	s_waitcnt vmcnt(0)
	v_add_u32_e32 v253, 0x680, v253
	v_mov_b32_e32 v2, s67
	ds_write_b32 v2, v253
.LppA_pr:
	s_or_b64 exec, exec, s[2:3]
	s_waitcnt lgkmcnt(0)
	s_barrier
	v_mov_b32_e32 v2, s67
	ds_read_b32 v2, v2
	s_waitcnt lgkmcnt(0)
	v_readfirstlane_b32 s30, v2
	s_nop 1
	v_writelane_b32 v255, s30, 22
	s_mov_b32 s16, 2
	s_barrier
	s_branch .LBB0_538

.LBB0_537:
	s_waitcnt lgkmcnt(0)
	v_readlane_b32 s30, v255, 22
	v_readlane_b32 s31, v255, 23
	s_nop 1
	v_writelane_b32 v255, s31, 22
	s_add_i32 s16, s16, 1
	s_barrier
	s_cmp_gt_i32 s30, 0x168f
	s_cbranch_scc1 .LBB0_690
.LBB0_538:
	s_mov_b32 s19, s20
	s_mov_b32 s10, s84
	s_mov_b32 s78, s21
	s_mov_b32 s69, s13
	s_mov_b32 s12, s18
	s_mov_b32 s68, s11
	s_mov_b64 s[80:81], s[82:83]
	s_waitcnt vmcnt(0)
	v_mov_b32_e32 v2, v112
	v_mov_b32_e32 v3, v113
	v_mov_b32_e32 v4, v114
	v_mov_b32_e32 v5, v115
	v_mov_b32_e32 v6, v116
	v_mov_b32_e32 v7, v117
	v_mov_b32_e32 v8, v118
	v_mov_b32_e32 v9, v119
	v_mov_b32_e32 v10, v120
	v_mov_b32_e32 v11, v121
	v_mov_b32_e32 v12, v122
	v_mov_b32_e32 v13, v123
	v_mov_b32_e32 v14, v124
	v_mov_b32_e32 v15, v125
	v_mov_b32_e32 v16, v126
	v_mov_b32_e32 v17, v127
	v_mov_b32_e32 v18, v128
	v_mov_b32_e32 v19, v129
	v_mov_b32_e32 v20, v130
	v_mov_b32_e32 v21, v131
	v_mov_b32_e32 v22, v132
	v_mov_b32_e32 v23, v133
	v_mov_b32_e32 v24, v134
	v_mov_b32_e32 v25, v135
	v_mov_b32_e32 v26, v136
	v_mov_b32_e32 v27, v137
	v_mov_b32_e32 v28, v138
	v_mov_b32_e32 v29, v139
	v_mov_b32_e32 v30, v140
	v_mov_b32_e32 v31, v141
	v_mov_b32_e32 v32, v142
	v_mov_b32_e32 v33, v143
	v_mov_b32_e32 v34, v144
	v_mov_b32_e32 v35, v145
	v_mov_b32_e32 v36, v146
	v_mov_b32_e32 v37, v147
	v_mov_b32_e32 v38, v148
	v_mov_b32_e32 v39, v149
	v_mov_b32_e32 v40, v150
	v_mov_b32_e32 v41, v151
	v_mov_b32_e32 v42, v152
	v_mov_b32_e32 v43, v153
	v_mov_b32_e32 v44, v154
	v_mov_b32_e32 v45, v155
	v_mov_b32_e32 v46, v156
	v_mov_b32_e32 v47, v157
	v_mov_b32_e32 v48, v158
	v_mov_b32_e32 v49, v159
	v_mov_b32_e32 v50, v160
	v_mov_b32_e32 v51, v161
	v_mov_b32_e32 v52, v162
	v_mov_b32_e32 v53, v163
	v_mov_b32_e32 v54, v164
	v_mov_b32_e32 v55, v165
	v_mov_b32_e32 v56, v166
	v_mov_b32_e32 v57, v167
	v_mov_b32_e32 v58, v168
	v_mov_b32_e32 v59, v169
	v_mov_b32_e32 v60, v170
	v_mov_b32_e32 v61, v171
	v_mov_b32_e32 v62, v172
	v_mov_b32_e32 v63, v173
	v_mov_b32_e32 v64, v174
	v_mov_b32_e32 v65, v175
	s_cmp_gt_u32 s16, 20
	s_cbranch_scc1 .LppA_nc
	s_and_saveexec_b64 s[2:3], s[0:1]
	s_cbranch_execz .LppA_cr
	v_readlane_b32 s30, v254, 52
	v_readlane_b32 s31, v254, 53
	v_mov_b32_e32 v253, 1
	s_nop 4
	global_atomic_add v253, v75, v253, s[30:31] offset:1280 sc0

.LppA_nc:
	v_readlane_b32 s30, v255, 22
	s_nop 3
	s_cmp_gt_i32 s30, 0x168f
	s_cbranch_scc1 .LppA_sk
	s_mov_b32 s23, s30
	s_cmpk_gt_i32 s23, 0x67f
	s_mov_b64 s[28:29], -1
	s_cbranch_scc0 .LBB0_576
	s_cmpk_gt_u32 s23, 0xa9f
	s_cbranch_scc0 .LBB0_565
	s_add_i32 s11, s23, 0xfffff560
	s_bfe_u32 s13, s11, 0x100007
	s_mulk_i32 s13, 0x2493
	s_lshr_b32 s21, s13, 16
	s_mul_i32 s20, s21, 0xfffffc80
	s_add_i32 s20, s20, s11
	s_cmpk_gt_i32 s20, 0x1bf
	s_mul_hi_u32 s24, s21, 0x3800000
	s_mul_i32 s25, s21, 0x3800000
	s_cbranch_scc0 .LBB0_562
	s_cmpk_gt_u32 s20, 0x37f
	s_cbranch_scc0 .LBB0_560
	v_readlane_b32 s36, v254, 38
	s_add_i32 s22, s20, 0xfffffc80
	v_readlane_b32 s46, v254, 48
	v_readlane_b32 s47, v254, 49
	s_add_u32 s34, s46, s25
	s_addc_u32 s35, s47, s24
	s_mul_i32 s11, s21, 0xe00000
	s_add_u32 s82, s17, s11
	v_readlane_b32 s37, v254, 39
	v_readlane_b32 s38, v254, 40
	v_readlane_b32 s39, v254, 41
	v_readlane_b32 s40, v254, 42
	v_readlane_b32 s41, v254, 43
	v_readlane_b32 s42, v254, 44
	v_readlane_b32 s43, v254, 45
	v_readlane_b32 s44, v254, 46
	v_readlane_b32 s45, v254, 47
	v_readlane_b32 s48, v254, 50
	v_readlane_b32 s49, v254, 51
	v_readlane_b32 s50, v254, 52
	v_readlane_b32 s51, v254, 53
	s_addc_u32 s83, s53, 0
	s_mov_b64 s[28:29], 0

.LBB0_590:
	s_lshr_b32 s21, s74, 7
	s_waitcnt vmcnt(16)
	v_cvt_f32_u32_e32 v112, s21
	s_sub_i32 s25, 0, s21
	s_abs_i32 s24, s22
	s_ashr_i32 s23, s22, 31
	v_rcp_iflag_f32_e32 v112, v112
	v_lshlrev_b32_e32 v74, 2, v192
	v_mul_f32_e32 v112, 0x4f7ffffe, v112
	v_cvt_u32_f32_e32 v112, v112
	s_nop 0
	v_readfirstlane_b32 s26, v112
	s_mul_i32 s25, s25, s26
	s_mul_hi_u32 s25, s26, s25
	s_add_i32 s26, s26, s25
	s_mul_hi_u32 s25, s24, s26
	s_mul_i32 s26, s25, s21
	s_sub_i32 s24, s24, s26
	s_add_i32 s27, s25, 1
	s_sub_i32 s26, s24, s21
	s_cmp_ge_u32 s24, s21
	s_cselect_b32 s25, s27, s25
	s_cselect_b32 s24, s26, s24
	s_add_i32 s26, s25, 1
	s_cmp_ge_u32 s24, s21
	s_cselect_b32 s24, s26, s25
	s_xor_b32 s24, s24, s23
	s_sub_i32 s23, s24, s23
	s_mul_i32 s24, s23, s21
	s_lshl_b32 s21, s23, 8
	s_sub_i32 s22, s22, s24
	v_or_b32_e32 v112, s21, v196
	s_ashr_i32 s23, s21, 31
	s_lshl_b32 s84, s22, 7
	s_mul_i32 s24, s23, s74
	v_mad_u64_u32 v[112:113], s[22:23], v112, s74, 0
	v_add_u32_e32 v113, s24, v113
	v_lshl_add_u64 v[112:113], v[112:113], 2, s[34:35]
	s_ashr_i32 s85, s84, 31
	v_lshl_add_u64 v[112:113], s[84:85], 2, v[112:113]
	v_lshl_add_u64 v[112:113], v[112:113], 0, v[74:75]
	s_lshl_b64 s[22:23], s[74:75], 2
	s_waitcnt vmcnt(14)
	v_lshl_add_u64 v[120:121], v[112:113], 0, s[22:23]
	global_load_dwordx4 v[112:115], v[112:113], off nt
	s_nop 0
	global_load_dwordx4 v[116:119], v[120:121], off nt
	v_lshl_add_u64 v[120:121], v[120:121], 0, s[22:23]
	s_waitcnt vmcnt(14)
	v_lshl_add_u64 v[128:129], v[120:121], 0, s[22:23]
	global_load_dwordx4 v[120:123], v[120:121], off nt
	s_nop 0
	global_load_dwordx4 v[124:127], v[128:129], off nt
	v_lshl_add_u64 v[128:129], v[128:129], 0, s[22:23]
	s_waitcnt vmcnt(14)
	v_lshl_add_u64 v[136:137], v[128:129], 0, s[22:23]
	global_load_dwordx4 v[128:131], v[128:129], off nt
	s_nop 0
	global_load_dwordx4 v[132:135], v[136:137], off nt
	v_lshl_add_u64 v[136:137], v[136:137], 0, s[22:23]
	s_waitcnt vmcnt(14)
	v_lshl_add_u64 v[144:145], v[136:137], 0, s[22:23]
	s_waitcnt vmcnt(13)
	v_lshl_add_u64 v[148:149], v[144:145], 0, s[22:23]
	s_waitcnt vmcnt(12)
	v_lshl_add_u64 v[152:153], v[148:149], 0, s[22:23]
	s_waitcnt vmcnt(11)
	v_lshl_add_u64 v[156:157], v[152:153], 0, s[22:23]
	s_waitcnt vmcnt(10)
	v_lshl_add_u64 v[160:161], v[156:157], 0, s[22:23]
	s_waitcnt vmcnt(9)
	v_lshl_add_u64 v[164:165], v[160:161], 0, s[22:23]
	s_waitcnt vmcnt(8)
	v_lshl_add_u64 v[168:169], v[164:165], 0, s[22:23]
	s_waitcnt vmcnt(7)
	v_lshl_add_u64 v[172:173], v[168:169], 0, s[22:23]
	global_load_dwordx4 v[136:139], v[136:137], off nt
	s_nop 0
	global_load_dwordx4 v[140:143], v[144:145], off nt
	s_nop 0
	global_load_dwordx4 v[144:147], v[148:149], off nt
	s_nop 0
	global_load_dwordx4 v[148:151], v[152:153], off nt
	s_nop 0
	global_load_dwordx4 v[152:155], v[156:157], off nt
	s_nop 0
	global_load_dwordx4 v[156:159], v[160:161], off nt
	s_nop 0
	global_load_dwordx4 v[160:163], v[164:165], off nt
	s_nop 0
	global_load_dwordx4 v[164:167], v[168:169], off nt
	s_nop 0
	global_load_dwordx4 v[168:171], v[172:173], off nt
	v_lshl_add_u64 v[172:173], v[172:173], 0, s[22:23]
	global_load_dwordx4 v[172:175], v[172:173], off nt
.LppA_sk:
	s_mov_b64 s[30:31], -1
	s_mov_b64 s[2:3], 0
	s_cmp_lt_i32 s19, 2
	s_mov_b64 s[28:29], 0
	s_cbranch_scc1 .LBB0_545
	s_cmp_eq_u32 s19, 2
	s_mov_b64 s[28:29], -1
	s_cbranch_scc0 .LBB0_541
	v_mul_f32_e32 v74, 0x44800000, v14
	v_mul_f32_e32 v69, 0x44800000, v10
	v_med3_f32 v86, v74, s66, v71
	v_mul_f32_e32 v74, 0x44800000, v26
	v_med3_f32 v82, v69, s66, v71
	v_mul_f32_e32 v77, 0x44800000, v30
	v_med3_f32 v83, v74, s66, v71
	v_mul_f32_e32 v67, 0x44800000, v6
	v_mul_f32_e32 v69, 0x44800000, v22
	v_med3_f32 v87, v77, s66, v71
	v_pk_add_f32 v[82:83], v[82:83], s[72:73] op_sel_hi:[1,0]
	v_mul_f32_e32 v66, 0x44800000, v2
	v_med3_f32 v68, v67, s66, v71
	v_mul_f32_e32 v67, 0x44800000, v18
	v_med3_f32 v69, v69, s66, v71
	v_pk_add_f32 v[86:87], v[86:87], s[72:73] op_sel_hi:[1,0]
	v_lshlrev_b32_e32 v74, 16, v83
	v_lshlrev_b32_e32 v77, 16, v82
	v_med3_f32 v66, v66, s66, v71
	v_med3_f32 v67, v67, s66, v71
	v_pk_add_f32 v[68:69], v[68:69], s[72:73] op_sel_hi:[1,0]
	v_and_b32_e32 v74, 0xff0000, v74
	v_and_b32_e32 v77, 0xff0000, v77
	v_lshlrev_b32_e32 v79, 24, v87
	v_lshlrev_b32_e32 v82, 24, v86
	v_pk_add_f32 v[66:67], v[66:67], s[72:73] op_sel_hi:[1,0]
	v_lshlrev_b32_e32 v69, 8, v69
	v_or_b32_e32 v74, v74, v79
	v_or_b32_e32 v77, v77, v82
	v_and_b32_e32 v69, 0xff00, v69
	v_or_b32_sdwa v67, v74, v67 dst_sel:DWORD dst_unused:UNUSED_PAD src0_sel:DWORD src1_sel:BYTE_0
	v_or_b32_sdwa v66, v77, v66 dst_sel:DWORD dst_unused:UNUSED_PAD src0_sel:DWORD src1_sel:BYTE_0
	v_mul_f32_e32 v74, 0x44800000, v42
	v_mul_f32_e32 v77, 0x44800000, v46
	v_or_b32_e32 v67, v67, v69
	v_mul_f32_e32 v69, 0x44800000, v38
	v_med3_f32 v86, v74, s66, v71
	v_med3_f32 v88, v77, s66, v71
	v_mul_f32_e32 v74, 0x44800000, v54
	v_mul_f32_e32 v77, 0x44800000, v58
	v_lshlrev_b32_e32 v68, 8, v68
	v_med3_f32 v82, v69, s66, v71
	v_mul_f32_e32 v79, 0x44800000, v62
	v_med3_f32 v83, v74, s66, v71
	v_med3_f32 v87, v77, s66, v71
	v_and_b32_e32 v68, 0xff00, v68
	v_med3_f32 v89, v79, s66, v71
	v_pk_add_f32 v[82:83], v[82:83], s[72:73] op_sel_hi:[1,0]
	v_pk_add_f32 v[86:87], v[86:87], s[72:73] op_sel_hi:[1,0]
	v_or_b32_e32 v66, v66, v68
	v_mul_f32_e32 v68, 0x44800000, v34
	v_mul_f32_e32 v69, 0x44800000, v50
	v_pk_add_f32 v[88:89], v[88:89], s[72:73] op_sel_hi:[1,0]
	v_lshlrev_b32_e32 v77, 8, v82
	v_lshlrev_b32_e32 v79, 16, v87
	v_lshlrev_b32_e32 v82, 16, v86
	v_med3_f32 v68, v68, s66, v71
	v_med3_f32 v69, v69, s66, v71
	v_lshlrev_b32_e32 v74, 8, v83
	v_and_b32_e32 v79, 0xff0000, v79
	v_and_b32_e32 v82, 0xff0000, v82
	v_lshlrev_b32_e32 v83, 24, v89
	v_lshlrev_b32_e32 v85, 24, v88
	v_pk_add_f32 v[68:69], v[68:69], s[72:73] op_sel_hi:[1,0]
	v_or_b32_e32 v79, v79, v83
	v_or_b32_e32 v82, v82, v85
	v_and_b32_e32 v74, 0xff00, v74
	v_and_b32_e32 v77, 0xff00, v77
	v_or_b32_sdwa v69, v79, v69 dst_sel:DWORD dst_unused:UNUSED_PAD src0_sel:DWORD src1_sel:BYTE_0
	v_or_b32_sdwa v68, v82, v68 dst_sel:DWORD dst_unused:UNUSED_PAD src0_sel:DWORD src1_sel:BYTE_0
	v_or_b32_e32 v69, v69, v74
	v_or_b32_e32 v68, v68, v77
	v_add_u32_e32 v74, v199, v198
	v_mul_f32_e32 v77, 0x44800000, v15
	ds_write_b128 v74, v[66:69]
	v_mul_f32_e32 v69, 0x44800000, v11
	v_med3_f32 v86, v77, s66, v71
	v_mul_f32_e32 v77, 0x44800000, v27
	v_med3_f32 v82, v69, s66, v71
	v_mul_f32_e32 v79, 0x44800000, v31
	v_med3_f32 v83, v77, s66, v71
	v_mul_f32_e32 v67, 0x44800000, v7
	v_mul_f32_e32 v69, 0x44800000, v23
	v_med3_f32 v87, v79, s66, v71
	v_pk_add_f32 v[82:83], v[82:83], s[72:73] op_sel_hi:[1,0]
	v_mul_f32_e32 v66, 0x44800000, v3
	v_med3_f32 v68, v67, s66, v71
	v_mul_f32_e32 v67, 0x44800000, v19
	v_med3_f32 v69, v69, s66, v71
	v_pk_add_f32 v[86:87], v[86:87], s[72:73] op_sel_hi:[1,0]
	v_lshlrev_b32_e32 v77, 16, v83
	v_lshlrev_b32_e32 v79, 16, v82
	v_med3_f32 v66, v66, s66, v71
	v_med3_f32 v67, v67, s66, v71
	v_pk_add_f32 v[68:69], v[68:69], s[72:73] op_sel_hi:[1,0]
	v_and_b32_e32 v77, 0xff0000, v77
	v_and_b32_e32 v79, 0xff0000, v79
	v_lshlrev_b32_e32 v82, 24, v87
	v_lshlrev_b32_e32 v83, 24, v86
	v_pk_add_f32 v[66:67], v[66:67], s[72:73] op_sel_hi:[1,0]
	v_lshlrev_b32_e32 v69, 8, v69
	v_or_b32_e32 v77, v77, v82
	v_or_b32_e32 v79, v79, v83
	v_and_b32_e32 v69, 0xff00, v69
	v_or_b32_sdwa v67, v77, v67 dst_sel:DWORD dst_unused:UNUSED_PAD src0_sel:DWORD src1_sel:BYTE_0
	v_or_b32_sdwa v66, v79, v66 dst_sel:DWORD dst_unused:UNUSED_PAD src0_sel:DWORD src1_sel:BYTE_0
	v_mul_f32_e32 v77, 0x44800000, v43
	v_mul_f32_e32 v79, 0x44800000, v47
	v_or_b32_e32 v67, v67, v69
	v_mul_f32_e32 v69, 0x44800000, v39
	v_med3_f32 v86, v77, s66, v71
	v_med3_f32 v88, v79, s66, v71
	v_mul_f32_e32 v77, 0x44800000, v55
	v_mul_f32_e32 v79, 0x44800000, v59
	v_lshlrev_b32_e32 v68, 8, v68
	v_med3_f32 v82, v69, s66, v71
	v_mul_f32_e32 v85, 0x44800000, v63
	v_med3_f32 v83, v77, s66, v71
	v_med3_f32 v87, v79, s66, v71
	v_and_b32_e32 v68, 0xff00, v68
	v_med3_f32 v89, v85, s66, v71
	v_pk_add_f32 v[82:83], v[82:83], s[72:73] op_sel_hi:[1,0]
	v_pk_add_f32 v[86:87], v[86:87], s[72:73] op_sel_hi:[1,0]
	v_or_b32_e32 v66, v66, v68
	v_mul_f32_e32 v68, 0x44800000, v35
	v_mul_f32_e32 v69, 0x44800000, v51
	v_pk_add_f32 v[88:89], v[88:89], s[72:73] op_sel_hi:[1,0]
	v_lshlrev_b32_e32 v77, 8, v83
	v_lshlrev_b32_e32 v79, 8, v82
	v_lshlrev_b32_e32 v82, 16, v87
	v_lshlrev_b32_e32 v83, 16, v86
	v_med3_f32 v68, v68, s66, v71
	v_med3_f32 v69, v69, s66, v71
	v_and_b32_e32 v82, 0xff0000, v82
	v_and_b32_e32 v83, 0xff0000, v83
	v_lshlrev_b32_e32 v85, 24, v89
	v_lshlrev_b32_e32 v86, 24, v88
	v_pk_add_f32 v[68:69], v[68:69], s[72:73] op_sel_hi:[1,0]
	v_or_b32_e32 v82, v82, v85
	v_or_b32_e32 v83, v83, v86
	v_and_b32_e32 v77, 0xff00, v77
	v_and_b32_e32 v79, 0xff00, v79
	v_or_b32_sdwa v69, v82, v69 dst_sel:DWORD dst_unused:UNUSED_PAD src0_sel:DWORD src1_sel:BYTE_0
	v_or_b32_sdwa v68, v83, v68 dst_sel:DWORD dst_unused:UNUSED_PAD src0_sel:DWORD src1_sel:BYTE_0
	v_or_b32_e32 v69, v69, v77
	v_or_b32_e32 v68, v68, v79
	v_mul_f32_e32 v77, 0x44800000, v16
	ds_write_b128 v74, v[66:69] offset:528
	v_mul_f32_e32 v69, 0x44800000, v12
	v_med3_f32 v86, v77, s66, v71
	v_mul_f32_e32 v77, 0x44800000, v28
	v_med3_f32 v82, v69, s66, v71
	v_mul_f32_e32 v79, 0x44800000, v32
	v_med3_f32 v83, v77, s66, v71
	v_mul_f32_e32 v67, 0x44800000, v8
	v_mul_f32_e32 v69, 0x44800000, v24
	v_med3_f32 v87, v79, s66, v71
	v_pk_add_f32 v[82:83], v[82:83], s[72:73] op_sel_hi:[1,0]
	v_mul_f32_e32 v66, 0x44800000, v4
	v_med3_f32 v68, v67, s66, v71
	v_mul_f32_e32 v67, 0x44800000, v20
	v_med3_f32 v69, v69, s66, v71
	v_pk_add_f32 v[86:87], v[86:87], s[72:73] op_sel_hi:[1,0]
	v_lshlrev_b32_e32 v77, 16, v83
	v_lshlrev_b32_e32 v79, 16, v82
	v_med3_f32 v66, v66, s66, v71
	v_med3_f32 v67, v67, s66, v71
	v_pk_add_f32 v[68:69], v[68:69], s[72:73] op_sel_hi:[1,0]
	v_and_b32_e32 v77, 0xff0000, v77
	v_and_b32_e32 v79, 0xff0000, v79
	v_lshlrev_b32_e32 v82, 24, v87
	v_lshlrev_b32_e32 v83, 24, v86
	v_pk_add_f32 v[66:67], v[66:67], s[72:73] op_sel_hi:[1,0]
	v_lshlrev_b32_e32 v69, 8, v69
	v_or_b32_e32 v77, v77, v82
	v_or_b32_e32 v79, v79, v83
	v_and_b32_e32 v69, 0xff00, v69
	v_or_b32_sdwa v67, v77, v67 dst_sel:DWORD dst_unused:UNUSED_PAD src0_sel:DWORD src1_sel:BYTE_0
	v_or_b32_sdwa v66, v79, v66 dst_sel:DWORD dst_unused:UNUSED_PAD src0_sel:DWORD src1_sel:BYTE_0
	v_mul_f32_e32 v77, 0x44800000, v44
	v_mul_f32_e32 v79, 0x44800000, v48
	v_or_b32_e32 v67, v67, v69
	v_mul_f32_e32 v69, 0x44800000, v40
	v_med3_f32 v86, v77, s66, v71
	v_med3_f32 v88, v79, s66, v71
	v_mul_f32_e32 v77, 0x44800000, v56
	v_mul_f32_e32 v79, 0x44800000, v60
	v_lshlrev_b32_e32 v68, 8, v68
	v_med3_f32 v82, v69, s66, v71
	v_mul_f32_e32 v85, 0x44800000, v64
	v_med3_f32 v83, v77, s66, v71
	v_med3_f32 v87, v79, s66, v71
	v_and_b32_e32 v68, 0xff00, v68
	v_med3_f32 v89, v85, s66, v71
	v_pk_add_f32 v[82:83], v[82:83], s[72:73] op_sel_hi:[1,0]
	v_pk_add_f32 v[86:87], v[86:87], s[72:73] op_sel_hi:[1,0]
	v_or_b32_e32 v66, v66, v68
	v_mul_f32_e32 v68, 0x44800000, v36
	v_mul_f32_e32 v69, 0x44800000, v52
	v_pk_add_f32 v[88:89], v[88:89], s[72:73] op_sel_hi:[1,0]
	v_lshlrev_b32_e32 v77, 8, v83
	v_lshlrev_b32_e32 v79, 8, v82
	v_lshlrev_b32_e32 v82, 16, v87
	v_lshlrev_b32_e32 v83, 16, v86
	v_med3_f32 v68, v68, s66, v71
	v_med3_f32 v69, v69, s66, v71
	v_and_b32_e32 v82, 0xff0000, v82
	v_and_b32_e32 v83, 0xff0000, v83
	v_lshlrev_b32_e32 v85, 24, v89
	v_lshlrev_b32_e32 v86, 24, v88
	v_pk_add_f32 v[68:69], v[68:69], s[72:73] op_sel_hi:[1,0]
	v_or_b32_e32 v82, v82, v85
	v_or_b32_e32 v83, v83, v86
	v_and_b32_e32 v77, 0xff00, v77
	v_and_b32_e32 v79, 0xff00, v79
	v_or_b32_sdwa v69, v82, v69 dst_sel:DWORD dst_unused:UNUSED_PAD src0_sel:DWORD src1_sel:BYTE_0
	v_or_b32_sdwa v68, v83, v68 dst_sel:DWORD dst_unused:UNUSED_PAD src0_sel:DWORD src1_sel:BYTE_0
	v_or_b32_e32 v69, v69, v77
	v_or_b32_e32 v68, v68, v79
	v_mul_f32_e32 v77, 0x44800000, v17
	ds_write_b128 v74, v[66:69] offset:1056
	v_mul_f32_e32 v69, 0x44800000, v13
	v_med3_f32 v86, v77, s66, v71
	v_mul_f32_e32 v77, 0x44800000, v29
	v_med3_f32 v82, v69, s66, v71
	v_mul_f32_e32 v79, 0x44800000, v33
	v_med3_f32 v83, v77, s66, v71
	v_mul_f32_e32 v67, 0x44800000, v9
	v_mul_f32_e32 v69, 0x44800000, v25
	v_med3_f32 v87, v79, s66, v71
	v_pk_add_f32 v[82:83], v[82:83], s[72:73] op_sel_hi:[1,0]
	v_mul_f32_e32 v66, 0x44800000, v5
	v_med3_f32 v68, v67, s66, v71
	v_mul_f32_e32 v67, 0x44800000, v21
	v_med3_f32 v69, v69, s66, v71
	v_pk_add_f32 v[86:87], v[86:87], s[72:73] op_sel_hi:[1,0]
	v_lshlrev_b32_e32 v77, 16, v83
	v_lshlrev_b32_e32 v79, 16, v82
	v_med3_f32 v66, v66, s66, v71
	v_med3_f32 v67, v67, s66, v71
	v_pk_add_f32 v[68:69], v[68:69], s[72:73] op_sel_hi:[1,0]
	v_and_b32_e32 v77, 0xff0000, v77
	v_and_b32_e32 v79, 0xff0000, v79
	v_lshlrev_b32_e32 v82, 24, v87
	v_lshlrev_b32_e32 v83, 24, v86
	v_pk_add_f32 v[66:67], v[66:67], s[72:73] op_sel_hi:[1,0]
	v_lshlrev_b32_e32 v69, 8, v69
	v_or_b32_e32 v77, v77, v82
	v_or_b32_e32 v79, v79, v83
	v_and_b32_e32 v69, 0xff00, v69
	v_or_b32_sdwa v67, v77, v67 dst_sel:DWORD dst_unused:UNUSED_PAD src0_sel:DWORD src1_sel:BYTE_0
	v_or_b32_sdwa v66, v79, v66 dst_sel:DWORD dst_unused:UNUSED_PAD src0_sel:DWORD src1_sel:BYTE_0
	v_mul_f32_e32 v77, 0x44800000, v45
	v_mul_f32_e32 v79, 0x44800000, v49
	v_or_b32_e32 v67, v67, v69
	v_mul_f32_e32 v69, 0x44800000, v41
	v_med3_f32 v86, v77, s66, v71
	v_med3_f32 v88, v79, s66, v71
	v_mul_f32_e32 v77, 0x44800000, v57
	v_mul_f32_e32 v79, 0x44800000, v61
	v_lshlrev_b32_e32 v68, 8, v68
	v_med3_f32 v82, v69, s66, v71
	v_mul_f32_e32 v85, 0x44800000, v65
	v_med3_f32 v83, v77, s66, v71
	v_med3_f32 v87, v79, s66, v71
	v_and_b32_e32 v68, 0xff00, v68
	v_med3_f32 v89, v85, s66, v71
	v_pk_add_f32 v[82:83], v[82:83], s[72:73] op_sel_hi:[1,0]
	v_pk_add_f32 v[86:87], v[86:87], s[72:73] op_sel_hi:[1,0]
	v_or_b32_e32 v66, v66, v68
	v_mul_f32_e32 v68, 0x44800000, v37
	v_mul_f32_e32 v69, 0x44800000, v53
	v_pk_add_f32 v[88:89], v[88:89], s[72:73] op_sel_hi:[1,0]
	v_lshlrev_b32_e32 v77, 8, v83
	v_lshlrev_b32_e32 v79, 8, v82
	v_lshlrev_b32_e32 v82, 16, v87
	v_lshlrev_b32_e32 v83, 16, v86
	v_med3_f32 v68, v68, s66, v71
	v_med3_f32 v69, v69, s66, v71
	v_and_b32_e32 v82, 0xff0000, v82
	v_and_b32_e32 v83, 0xff0000, v83
	v_lshlrev_b32_e32 v85, 24, v89
	v_lshlrev_b32_e32 v86, 24, v88
	v_pk_add_f32 v[68:69], v[68:69], s[72:73] op_sel_hi:[1,0]
	v_or_b32_e32 v82, v82, v85
	v_or_b32_e32 v83, v83, v86
	v_and_b32_e32 v77, 0xff00, v77
	v_and_b32_e32 v79, 0xff00, v79
	v_or_b32_sdwa v69, v82, v69 dst_sel:DWORD dst_unused:UNUSED_PAD src0_sel:DWORD src1_sel:BYTE_0
	v_or_b32_sdwa v68, v83, v68 dst_sel:DWORD dst_unused:UNUSED_PAD src0_sel:DWORD src1_sel:BYTE_0
	v_or_b32_e32 v69, v69, v77
	v_or_b32_e32 v68, v68, v79
	ds_write_b128 v74, v[66:69] offset:1584
	s_mov_b64 s[28:29], 0

.LBB0_543:
	v_mul_f32_e32 v67, 0x43800000, v2
	v_mul_f32_e32 v68, 0x43800000, v6
	v_mov_b32_e32 v66, v75
	v_cvt_pk_fp8_f32 v66, v67, v68
	v_mul_f32_e32 v67, 0x43800000, v10
	v_mul_f32_e32 v68, 0x43800000, v14
	v_mul_f32_e32 v69, 0x43800000, v22
	v_cvt_pk_fp8_f32 v66, v67, v68 op_sel:[0,0,1]
	v_mul_f32_e32 v68, 0x43800000, v18
	v_mov_b32_e32 v67, v75
	v_cvt_pk_fp8_f32 v67, v68, v69
	v_mul_f32_e32 v68, 0x43800000, v26
	v_mul_f32_e32 v69, 0x43800000, v30
	v_mul_f32_e32 v74, 0x43800000, v38
	v_cvt_pk_fp8_f32 v67, v68, v69 op_sel:[0,0,1]
	v_mul_f32_e32 v69, 0x43800000, v34
	v_mov_b32_e32 v68, v75
	v_cvt_pk_fp8_f32 v68, v69, v74
	v_mul_f32_e32 v69, 0x43800000, v42
	v_mul_f32_e32 v74, 0x43800000, v46
	v_mul_f32_e32 v77, 0x43800000, v54
	v_cvt_pk_fp8_f32 v68, v69, v74 op_sel:[0,0,1]
	v_mul_f32_e32 v74, 0x43800000, v50
	v_mov_b32_e32 v69, v75
	v_cvt_pk_fp8_f32 v69, v74, v77
	v_mul_f32_e32 v74, 0x43800000, v58
	v_mul_f32_e32 v77, 0x43800000, v62
	v_mul_f32_e32 v79, 0x43800000, v55
	v_cvt_pk_fp8_f32 v69, v74, v77 op_sel:[0,0,1]
	v_add_u32_e32 v74, v199, v198
	v_mul_f32_e32 v77, 0x43800000, v39
	ds_write_b128 v74, v[66:69]
	v_mul_f32_e32 v67, 0x43800000, v3
	v_mul_f32_e32 v68, 0x43800000, v7
	v_mov_b32_e32 v66, v75
	v_cvt_pk_fp8_f32 v66, v67, v68
	v_mul_f32_e32 v67, 0x43800000, v11
	v_mul_f32_e32 v68, 0x43800000, v15
	v_mul_f32_e32 v69, 0x43800000, v23
	v_cvt_pk_fp8_f32 v66, v67, v68 op_sel:[0,0,1]
	v_mul_f32_e32 v68, 0x43800000, v19
	v_mov_b32_e32 v67, v75
	v_cvt_pk_fp8_f32 v67, v68, v69
	v_mul_f32_e32 v68, 0x43800000, v27
	v_mul_f32_e32 v69, 0x43800000, v31
	v_cvt_pk_fp8_f32 v67, v68, v69 op_sel:[0,0,1]
	v_mul_f32_e32 v69, 0x43800000, v35
	v_mov_b32_e32 v68, v75
	v_cvt_pk_fp8_f32 v68, v69, v77
	v_mul_f32_e32 v69, 0x43800000, v43
	v_mul_f32_e32 v77, 0x43800000, v47
	v_cvt_pk_fp8_f32 v68, v69, v77 op_sel:[0,0,1]
	v_mul_f32_e32 v77, 0x43800000, v51
	v_mov_b32_e32 v69, v75
	v_cvt_pk_fp8_f32 v69, v77, v79
	v_mul_f32_e32 v77, 0x43800000, v59
	v_mul_f32_e32 v79, 0x43800000, v63
	v_cvt_pk_fp8_f32 v69, v77, v79 op_sel:[0,0,1]
	v_mul_f32_e32 v77, 0x43800000, v40
	v_mul_f32_e32 v79, 0x43800000, v56
	ds_write_b128 v74, v[66:69] offset:528
	v_mul_f32_e32 v67, 0x43800000, v4
	v_mul_f32_e32 v68, 0x43800000, v8
	v_mov_b32_e32 v66, v75
	v_cvt_pk_fp8_f32 v66, v67, v68
	v_mul_f32_e32 v67, 0x43800000, v12
	v_mul_f32_e32 v68, 0x43800000, v16
	v_mul_f32_e32 v69, 0x43800000, v24
	v_cvt_pk_fp8_f32 v66, v67, v68 op_sel:[0,0,1]
	v_mul_f32_e32 v68, 0x43800000, v20
	v_mov_b32_e32 v67, v75
	v_cvt_pk_fp8_f32 v67, v68, v69
	v_mul_f32_e32 v68, 0x43800000, v28
	v_mul_f32_e32 v69, 0x43800000, v32
	v_cvt_pk_fp8_f32 v67, v68, v69 op_sel:[0,0,1]
	v_mul_f32_e32 v69, 0x43800000, v36
	v_mov_b32_e32 v68, v75
	v_cvt_pk_fp8_f32 v68, v69, v77
	v_mul_f32_e32 v69, 0x43800000, v44
	v_mul_f32_e32 v77, 0x43800000, v48
	v_cvt_pk_fp8_f32 v68, v69, v77 op_sel:[0,0,1]
	v_mul_f32_e32 v77, 0x43800000, v52
	v_mov_b32_e32 v69, v75
	v_cvt_pk_fp8_f32 v69, v77, v79
	v_mul_f32_e32 v77, 0x43800000, v60
	v_mul_f32_e32 v79, 0x43800000, v64
	v_cvt_pk_fp8_f32 v69, v77, v79 op_sel:[0,0,1]
	v_mul_f32_e32 v77, 0x43800000, v41
	v_mul_f32_e32 v79, 0x43800000, v57
	ds_write_b128 v74, v[66:69] offset:1056
	v_mul_f32_e32 v67, 0x43800000, v5
	v_mul_f32_e32 v68, 0x43800000, v9
	v_mov_b32_e32 v66, v75
	v_cvt_pk_fp8_f32 v66, v67, v68
	v_mul_f32_e32 v67, 0x43800000, v13
	v_mul_f32_e32 v68, 0x43800000, v17
	v_mul_f32_e32 v69, 0x43800000, v25
	v_cvt_pk_fp8_f32 v66, v67, v68 op_sel:[0,0,1]
	v_mul_f32_e32 v68, 0x43800000, v21
	v_mov_b32_e32 v67, v75
	v_cvt_pk_fp8_f32 v67, v68, v69
	v_mul_f32_e32 v68, 0x43800000, v29
	v_mul_f32_e32 v69, 0x43800000, v33
	v_cvt_pk_fp8_f32 v67, v68, v69 op_sel:[0,0,1]
	v_mul_f32_e32 v69, 0x43800000, v37
	v_mov_b32_e32 v68, v75
	v_cvt_pk_fp8_f32 v68, v69, v77
	v_mul_f32_e32 v69, 0x43800000, v45
	v_mul_f32_e32 v77, 0x43800000, v49
	v_cvt_pk_fp8_f32 v68, v69, v77 op_sel:[0,0,1]
	v_mul_f32_e32 v77, 0x43800000, v53
	v_mov_b32_e32 v69, v75
	v_cvt_pk_fp8_f32 v69, v77, v79
	v_mul_f32_e32 v77, 0x43800000, v61
	v_mul_f32_e32 v79, 0x43800000, v65
	v_cvt_pk_fp8_f32 v69, v77, v79 op_sel:[0,0,1]
	ds_write_b128 v74, v[66:69] offset:1584
	s_cbranch_execz .LBB0_548

.LBB0_548:
	v_cvt_pk_bf16_f32 v66, v2, v6
	v_cvt_pk_bf16_f32 v67, v10, v14
	v_cvt_pk_bf16_f32 v68, v18, v22
	v_cvt_pk_bf16_f32 v69, v26, v30
	v_add_u32_e32 v74, v197, v198
	v_cvt_pk_bf16_f32 v86, v34, v38
	v_cvt_pk_bf16_f32 v87, v42, v46
	v_cvt_pk_bf16_f32 v88, v50, v54
	v_cvt_pk_bf16_f32 v89, v58, v62
	ds_write_b128 v74, v[66:69]
	ds_write_b128 v74, v[86:89] offset:16
	v_cvt_pk_bf16_f32 v66, v3, v7
	v_cvt_pk_bf16_f32 v67, v11, v15
	v_cvt_pk_bf16_f32 v68, v19, v23
	v_cvt_pk_bf16_f32 v69, v27, v31
	v_cvt_pk_bf16_f32 v86, v35, v39
	v_cvt_pk_bf16_f32 v87, v43, v47
	v_cvt_pk_bf16_f32 v88, v51, v55
	v_cvt_pk_bf16_f32 v89, v59, v63
	ds_write_b128 v74, v[66:69] offset:528
	ds_write_b128 v74, v[86:89] offset:544
	v_cvt_pk_bf16_f32 v66, v4, v8
	v_cvt_pk_bf16_f32 v67, v12, v16
	v_cvt_pk_bf16_f32 v68, v20, v24
	v_cvt_pk_bf16_f32 v69, v28, v32
	v_cvt_pk_bf16_f32 v86, v36, v40
	v_cvt_pk_bf16_f32 v87, v44, v48
	v_cvt_pk_bf16_f32 v88, v52, v56
	v_cvt_pk_bf16_f32 v89, v60, v64
	ds_write_b128 v74, v[66:69] offset:1056
	ds_write_b128 v74, v[86:89] offset:1072
	v_cvt_pk_bf16_f32 v66, v5, v9
	v_cvt_pk_bf16_f32 v67, v13, v17
	v_cvt_pk_bf16_f32 v68, v21, v25
	v_cvt_pk_bf16_f32 v69, v29, v33
	v_cvt_pk_bf16_f32 v86, v37, v41
	v_cvt_pk_bf16_f32 v87, v45, v49
	v_cvt_pk_bf16_f32 v88, v53, v57
	v_cvt_pk_bf16_f32 v89, v61, v65
	ds_write_b128 v74, v[66:69] offset:1584
	ds_write_b128 v74, v[86:89] offset:1600
	s_and_saveexec_b64 s[2:3], s[0:1]
	s_cbranch_execz .LBB0_554
.LBB0_549:
	s_cmp_gt_u32 s16, 20
	v_mov_b32_e32 v66, 0x1690
	s_cbranch_scc1 .LBB0_553
	s_mov_b64 s[30:31], exec
	v_mbcnt_lo_u32_b32 v66, s30, 0
	v_mbcnt_hi_u32_b32 v66, s31, v66
	v_cmp_eq_u32_e32 vcc, 0, v66
	s_and_saveexec_b64 s[28:29], vcc
	s_cbranch_execz .LBB0_552
	s_bcnt1_i32_b64 s31, s[30:31]
	v_readlane_b32 s36, v254, 38
	v_mov_b32_e32 v67, s31
	v_readlane_b32 s50, v254, 52
	v_readlane_b32 s51, v254, 53
	v_readlane_b32 s37, v254, 39
	v_readlane_b32 s38, v254, 40
	v_readlane_b32 s39, v254, 41
	v_readlane_b32 s40, v254, 42
	v_readlane_b32 s41, v254, 43
	v_readlane_b32 s42, v254, 44
	v_readlane_b32 s43, v254, 45
	v_readlane_b32 s44, v254, 46
	v_readlane_b32 s45, v254, 47
	v_readlane_b32 s46, v254, 48
	v_readlane_b32 s47, v254, 49
	v_readlane_b32 s48, v254, 50
	v_readlane_b32 s49, v254, 51
.LBB0_552:
	s_or_b64 exec, exec, s[28:29]
	v_readlane_b32 s30, v255, 22
	s_waitcnt vmcnt(16)
	s_nop 2
	s_cmp_gt_i32 s30, 0x168f
	s_cbranch_scc0 .LppA_w
	s_waitcnt vmcnt(0)
.LppA_w:
	v_readfirstlane_b32 s31, v253
	s_nop 1
	v_add_u32_e32 v66, s31, v66
	v_add_u32_e32 v66, 0x680, v66

.LBB0_554:
	s_or_b64 exec, exec, s[2:3]
	v_mov_b32_e32 v66, s67
	s_waitcnt lgkmcnt(0)
	s_waitcnt lgkmcnt(0)
	s_barrier
	ds_read_b32 v66, v66
	s_waitcnt lgkmcnt(0)
	v_readfirstlane_b32 s23, v66
	s_nop 1
	v_writelane_b32 v255, s23, 23
